# P2 postproj rewritten by hand: all row loads in flight at once, hoisted weights, DPP reductions
# speedup vs baseline: 1.0004x; 1.0004x over previous
; __device__ __forceinline__ void postproj_row(int R, int lane, const bf16* __restrict__ proj, const float* __restrict__ conv_w, const float* __restrict__ g_conv, ...
;     const bf16* pr = proj + (size_t)R * DINP;
;     const bool meta = R >= M; const int b = meta ? 0 : R / S, t = meta ? 0 : R % S, pos = meta ? R - M : t + NMETA;
;     {
;         const u32x2 w = *(const u32x2*)(pr + O_KV + lane * 4);
;         float f[4] = {__uint_as_float(w.x << 16), __uint_as_float(w.x & 0xffff0000u), __uint_as_float(w.y << 16), __uint_as_float(w.y & 0xffff0000u)};
;         const float ss = wave_sum(f[0] * f[0] + f[1] * f[1] + f[2] * f[2] + f[3] * f[3]);
;         const float rstd = rsqrtf(ss * (1.f / KVL) + EPS);
;         const f32x4 g = *(const f32x4*)(g_kv + lane * 4);
;         u32x2 o; o.x = pk2(f[0] * rstd * g.x, f[1] * rstd * g.y); o.y = pk2(f[2] * rstd * g.z, f[3] * rstd * g.w);
;         *(u32x2*)(kvn + (size_t)R * KVL + lane * 4) = o;
;     }
;     if (lane < 32) {
;         const float x1 = bf2f(pr[O_R + lane]), x2 = bf2f(pr[O_R + 32 + lane]);
;         const float cs = cosT[pos * 32 + lane], sn = sinT[pos * 32 + lane];
;         const bf16 o1 = f2bf(x1 * cs - x2 * sn), o2 = f2bf(x1 * sn + x2 * cs);
;         if (!meta) { bf16* d = kpe + (size_t)(b * LP + pos) * ROPE; d[lane] = o1; d[32 + lane] = o2; }
;         else { bf16* d0 = kpe + (size_t)(0 * LP + pos) * ROPE; bf16* d1 = kpe + (size_t)(1 * LP + pos) * ROPE; d0[lane] = o1; d0[32 + lane] = o2; d1[lane] = o1; d1[32 + lane] = o2; }
;     }
;     if (meta) return;
;     {
;         float f[8]; unpack8(*(const u32x4*)(pr + O_Q + lane * 8), f);
;         float ss = 0.f;
; #pragma unroll
;         for (int i = 0; i < 8; ++i) ss += f[i] * f[i];
;         const float rstd = rsqrtf(wave_sum(ss) * (1.f / QL) + EPS);
;         const f32x4 g0 = *(const f32x4*)(g_q + lane * 8), g1 = *(const f32x4*)(g_q + lane * 8 + 4);
;         u32x4 o; o.x = pk2(f[0] * rstd * g0.x, f[1] * rstd * g0.y); o.y = pk2(f[2] * rstd * g0.z, f[3] * rstd * g0.w);
;         o.z = pk2(f[4] * rstd * g1.x, f[5] * rstd * g1.y); o.w = pk2(f[6] * rstd * g1.z, f[7] * rstd * g1.w);
;         *(u32x4*)(qn + (size_t)R * QL + lane * 8) = o;
;     }
;     {
;         const int r1 = (t >= 1) ? R - 1 : M + 15, r2 = (t >= 2) ? R - 2 : (t == 1 ? M + 15 : M + 14);
;         const bf16* p1 = proj + (size_t)r1 * DINP; const bf16* p2 = proj + (size_t)r2 * DINP;
.LBB0_387:
	s_load_dwordx2 s[0:1], s[94:95], 0xb0
	s_waitcnt lgkmcnt(0)
	s_cmp_lt_i32 s0, 3
	s_cselect_b64 s[6:7], -1, 0
	s_and_b64 s[28:29], s[6:7], s[4:5]
	s_andn2_b64 vcc, exec, s[28:29]
	s_cbranch_vccnz .LBB0_400
	s_load_dwordx4 s[8:11], s[94:95], 0x20
	s_load_dwordx2 s[14:15], s[94:95], 0x38
	s_load_dwordx2 s[16:17], s[94:95], 0x48
	s_load_dwordx2 s[36:37], s[94:95], 0xa8
	v_and_b32_e32 v1, 63, v0
	v_readfirstlane_b32 s6, v0
	s_lshl_b32 s7, s2, 3
	s_lshl_b32 s30, s3, 3
	s_lshr_b32 s6, s6, 6
	s_add_i32 s42, s6, s7
	v_lshlrev_b32_e32 v2, 5, v1
	v_lshlrev_b32_e32 v3, 4, v1
	v_lshlrev_b32_e32 v4, 3, v1
	v_lshlrev_b32_e32 v5, 2, v1
	v_lshlrev_b32_e32 v6, 1, v1
	v_lshlrev_b32_e32 v7, 6, v1
	s_waitcnt lgkmcnt(0)
	s_add_u32 s18, s8, 0x1000
	s_addc_u32 s19, s9, 0
	s_add_u32 s20, s8, 0x2000
	s_addc_u32 s21, s9, 0
	global_load_dwordx4 v[8:11], v3, s[14:15]
	global_load_dwordx4 v[12:15], v2, s[10:11]
	global_load_dwordx4 v[16:19], v2, s[10:11] offset:16
	global_load_dwordx4 v[20:23], v7, s[16:17]
	global_load_dwordx4 v[24:27], v7, s[16:17] offset:16
	global_load_dwordx4 v[28:31], v7, s[16:17] offset:32
	global_load_dwordx4 v[32:35], v7, s[16:17] offset:48
	global_load_dwordx4 v[36:39], v7, s[8:9]
	global_load_dwordx4 v[40:43], v7, s[8:9] offset:16
	global_load_dwordx4 v[44:47], v7, s[8:9] offset:32
	global_load_dwordx4 v[48:51], v7, s[8:9] offset:48
	global_load_dwordx4 v[52:55], v7, s[18:19]
	global_load_dwordx4 v[56:59], v7, s[18:19] offset:16
	global_load_dwordx4 v[60:63], v7, s[18:19] offset:32
	global_load_dwordx4 v[64:67], v7, s[18:19] offset:48
	global_load_dwordx4 v[68:71], v7, s[20:21]
	global_load_dwordx4 v[72:75], v7, s[20:21] offset:16
	global_load_dwordx4 v[76:79], v7, s[20:21] offset:32
	global_load_dwordx4 v[80:83], v7, s[20:21] offset:48
	s_add_u32 s44, s36, 0x34000000
	s_addc_u32 s45, s37, 0
	s_add_u32 s46, s36, 0x38200000
	s_addc_u32 s47, s37, 0
	s_add_u32 s34, s36, 0x3a200000
	s_addc_u32 s35, s37, 0
	s_add_u32 s38, s36, 0x3aa00000
	s_addc_u32 s39, s37, 0
	s_add_u32 s40, s36, 0x3b200000
	s_addc_u32 s41, s37, 0
	s_add_u32 s26, s36, 0x41c00000
	s_addc_u32 s27, s37, 0
	s_cmpk_lt_i32 s42, 0x2000
	s_cbranch_scc0 .Lp2_meta_chk
.Lp2_loop:
	s_lshl_b32 s43, s42, 13
	s_add_u32 s48, s44, s43
	s_addc_u32 s49, s45, 0
	s_add_u32 s50, s48, 0x1000
	s_addc_u32 s51, s49, 0
	s_and_b32 s52, s42, 0xfff
	s_lshr_b32 s53, s42, 12
	s_add_i32 s54, s42, -1
	s_cmp_eq_u32 s52, 0
	s_cselect_b32 s54, 0x200f, s54
	s_add_i32 s56, s42, -2
	s_add_i32 s43, s52, 0x200e
	s_cmp_lt_u32 s52, 2
	s_cselect_b32 s56, s43, s56
	s_lshl_b32 s54, s54, 13
	s_lshl_b32 s56, s56, 13
	s_add_u32 s54, s54, 0x800
	s_add_u32 s56, s56, 0x800
	s_add_u32 s54, s44, s54
	s_addc_u32 s55, s45, 0
	s_add_u32 s56, s44, s56
	s_addc_u32 s57, s45, 0
	s_add_i32 s43, s52, 16
	s_lshl_b32 s58, s43, 7
	s_add_u32 s58, s40, s58
	s_addc_u32 s59, s41, 0
	s_add_u32 s4, s58, 0x100000
	s_addc_u32 s5, s59, 0
	global_load_dwordx4 v[108:111], v2, s[54:55]
	global_load_dwordx4 v[112:115], v2, s[54:55] offset:16
	global_load_dwordx4 v[116:119], v2, s[54:55] offset:2048
	global_load_dwordx4 v[120:123], v2, s[54:55] offset:2064
	global_load_dwordx4 v[124:127], v2, s[56:57]
	global_load_dwordx4 v[128:131], v2, s[56:57] offset:16
	global_load_dwordx4 v[132:135], v2, s[56:57] offset:2048
	global_load_dwordx4 v[136:139], v2, s[56:57] offset:2064
	global_load_dwordx4 v[84:87], v2, s[48:49]
	global_load_dwordx4 v[88:91], v2, s[48:49] offset:16
	global_load_dwordx4 v[92:95], v2, s[48:49] offset:2048
	global_load_dwordx4 v[96:99], v2, s[48:49] offset:2064
	global_load_dwordx4 v[100:103], v2, s[50:51]
	global_load_dwordx4 v[104:107], v2, s[50:51] offset:16
	global_load_dwordx4 v[140:143], v3, s[50:51] offset:2048
	global_load_dwordx2 v[144:145], v4, s[50:51] offset:3072
	global_load_ushort v146, v6, s[50:51] offset:3584
	global_load_ushort v147, v6, s[50:51] offset:3648
	global_load_dword v148, v5, s[58:59]
	global_load_dword v149, v5, s[4:5]
	s_lshl_b32 s43, s42, 12
	s_add_u32 s6, s46, s43
	s_addc_u32 s7, s47, 0
	s_lshl_b32 s43, s42, 10
	s_add_u32 s24, s34, s43
	s_addc_u32 s25, s35, 0
	s_lshl_b32 s43, s42, 9
	s_add_u32 s8, s38, s43
	s_addc_u32 s9, s39, 0
	s_mulk_i32 s53, 0x1080
	s_add_i32 s53, s53, s52
	s_add_i32 s53, s53, 16
	s_lshl_b32 s53, s53, 7
	s_add_u32 s10, s26, s53
	s_addc_u32 s11, s27, 0
	v_mov_b32_e32 v206, 0x358637bd
	s_waitcnt vmcnt(0)
; __device__ __forceinline__ void postproj_row(int R, int lane, const bf16* __restrict__ proj, const float* __restrict__ conv_w, const float* __restrict__ g_conv, ...
;     ...
;         const u32x2 w = *(const u32x2*)(pr + O_KV + lane * 4);
;         float f[4] = {__uint_as_float(w.x << 16), __uint_as_float(w.x & 0xffff0000u), __uint_as_float(w.y << 16), __uint_as_float(w.y & 0xffff0000u)};
;         const float ss = wave_sum(f[0] * f[0] + f[1] * f[1] + f[2] * f[2] + f[3] * f[3]);
;         const float rstd = rsqrtf(ss * (1.f / KVL) + EPS);
;         const f32x4 g = *(const f32x4*)(g_kv + lane * 4);
;         u32x2 o; o.x = pk2(f[0] * rstd * g.x, f[1] * rstd * g.y); o.y = pk2(f[2] * rstd * g.z, f[3] * rstd * g.w);
;         *(u32x2*)(kvn + (size_t)R * KVL + lane * 4) = o;
;     }
;     if (lane < 32) {
;         const float x1 = bf2f(pr[O_R + lane]), x2 = bf2f(pr[O_R + 32 + lane]);
;         const float cs = cosT[pos * 32 + lane], sn = sinT[pos * 32 + lane];
;         const bf16 o1 = f2bf(x1 * cs - x2 * sn), o2 = f2bf(x1 * sn + x2 * cs);
;         if (!meta) { bf16* d = kpe + (size_t)(b * LP + pos) * ROPE; d[lane] = o1; d[32 + lane] = o2; }
;         else { bf16* d0 = kpe + (size_t)(0 * LP + pos) * ROPE; bf16* d1 = kpe + (size_t)(1 * LP + pos) * ROPE; d0[lane] = o1; d0[32 + lane] = o2; d1[lane] = o1; d1[32 + lane] = o2; }
;     }
;     if (meta) return;
;     {
;         float f[8]; unpack8(*(const u32x4*)(pr + O_Q + lane * 8), f);
;         float ss = 0.f;
; #pragma unroll
;         for (int i = 0; i < 8; ++i) ss += f[i] * f[i];
;         const float rstd = rsqrtf(wave_sum(ss) * (1.f / QL) + EPS);
;         const f32x4 g0 = *(const f32x4*)(g_q + lane * 8), g1 = *(const f32x4*)(g_q + lane * 8 + 4);
;         u32x4 o; o.x = pk2(f[0] * rstd * g0.x, f[1] * rstd * g0.y); o.y = pk2(f[2] * rstd * g0.z, f[3] * rstd * g0.w);
;         o.z = pk2(f[4] * rstd * g1.x, f[5] * rstd * g1.y); o.w = pk2(f[6] * rstd * g1.z, f[7] * rstd * g1.w);
;         *(u32x4*)(qn + (size_t)R * QL + lane * 8) = o;
;     }
;     {
;         const int r1 = (t >= 1) ? R - 1 : M + 15, r2 = (t >= 2) ? R - 2 : (t == 1 ? M + 15 : M + 14);
;         const bf16* p1 = proj + (size_t)r1 * DINP; const bf16* p2 = proj + (size_t)r2 * DINP;
;         const int c0 = lane * 16;
;         float v[16]; float ss = 0.f;
; #pragma unroll
;         for (int hh = 0; hh < 2; ++hh) {
	v_lshlrev_b32_e32 v186, 16, v140
	v_and_b32_e32 v187, 0xffff0000, v140
	v_lshlrev_b32_e32 v188, 16, v141
	v_and_b32_e32 v189, 0xffff0000, v141
	v_lshlrev_b32_e32 v190, 16, v142
	v_and_b32_e32 v191, 0xffff0000, v142
	v_lshlrev_b32_e32 v192, 16, v143
	v_and_b32_e32 v193, 0xffff0000, v143
	v_mul_f32_e32 v194, v186, v186
	v_fmac_f32_e32 v194, v187, v187
	v_fmac_f32_e32 v194, v188, v188
	v_fmac_f32_e32 v194, v189, v189
	v_fmac_f32_e32 v194, v190, v190
	v_fmac_f32_e32 v194, v191, v191
	v_fmac_f32_e32 v194, v192, v192
	v_fmac_f32_e32 v194, v193, v193
	v_lshlrev_b32_e32 v196, 16, v144
	v_and_b32_e32 v197, 0xffff0000, v144
	v_lshlrev_b32_e32 v198, 16, v145
	v_and_b32_e32 v199, 0xffff0000, v145
	v_mul_f32_e32 v195, v196, v196
	v_fmac_f32_e32 v195, v197, v197
	v_fmac_f32_e32 v195, v198, v198
	v_fmac_f32_e32 v195, v199, v199
	s_nop 1
	v_add_f32_dpp v194, v194, v194 quad_perm:[1,0,3,2] row_mask:0xf bank_mask:0xf
	v_add_f32_dpp v195, v195, v195 quad_perm:[1,0,3,2] row_mask:0xf bank_mask:0xf
	s_nop 1
	v_add_f32_dpp v194, v194, v194 quad_perm:[2,3,0,1] row_mask:0xf bank_mask:0xf
	v_add_f32_dpp v195, v195, v195 quad_perm:[2,3,0,1] row_mask:0xf bank_mask:0xf
	s_nop 1
	v_add_f32_dpp v194, v194, v194 row_half_mirror row_mask:0xf bank_mask:0xf
	v_add_f32_dpp v195, v195, v195 row_half_mirror row_mask:0xf bank_mask:0xf
	s_nop 1
	v_add_f32_dpp v194, v194, v194 row_mirror row_mask:0xf bank_mask:0xf
	v_add_f32_dpp v195, v195, v195 row_mirror row_mask:0xf bank_mask:0xf
	s_nop 1
	v_add_f32_dpp v194, v194, v194 row_bcast:15 row_mask:0xa bank_mask:0xf
	v_add_f32_dpp v195, v195, v195 row_bcast:15 row_mask:0xa bank_mask:0xf
	s_nop 1
	v_add_f32_dpp v194, v194, v194 row_bcast:31 row_mask:0xc bank_mask:0xf
	v_add_f32_dpp v195, v195, v195 row_bcast:31 row_mask:0xc bank_mask:0xf
	v_lshlrev_b32_e32 v150, 16, v92
	v_and_b32_e32 v151, 0xffff0000, v92
	v_lshlrev_b32_e32 v152, 16, v100
	v_and_b32_e32 v153, 0xffff0000, v100
	v_pk_mul_f32 v[150:151], v[150:151], v[152:153]
	v_lshlrev_b32_e32 v152, 16, v108
	v_and_b32_e32 v153, 0xffff0000, v108
	v_lshlrev_b32_e32 v154, 16, v116
	v_and_b32_e32 v155, 0xffff0000, v116
	v_pk_mul_f32 v[152:153], v[152:153], v[154:155]
	v_lshlrev_b32_e32 v154, 16, v124
	v_and_b32_e32 v155, 0xffff0000, v124
	v_lshlrev_b32_e32 v156, 16, v132
	v_and_b32_e32 v157, 0xffff0000, v132
	v_pk_mul_f32 v[154:155], v[154:155], v[156:157]
	v_pk_mul_f32 v[152:153], v[52:53], v[152:153]
	v_pk_fma_f32 v[152:153], v[68:69], v[150:151], v[152:153]
	v_pk_fma_f32 v[152:153], v[36:37], v[154:155], v[152:153]
	v_lshlrev_b32_e32 v156, 16, v84
	v_and_b32_e32 v157, 0xffff0000, v84
	v_pk_mul_f32 v[160:161], v[156:157], v[152:153]
	v_mul_f32_e32 v158, v160, v160
	v_fmac_f32_e32 v158, v161, v161
	v_lshlrev_b32_e32 v150, 16, v93
	v_and_b32_e32 v151, 0xffff0000, v93
	v_lshlrev_b32_e32 v152, 16, v101
	v_and_b32_e32 v153, 0xffff0000, v101
	v_pk_mul_f32 v[150:151], v[150:151], v[152:153]
	v_lshlrev_b32_e32 v152, 16, v109
	v_and_b32_e32 v153, 0xffff0000, v109
	v_lshlrev_b32_e32 v154, 16, v117
	v_and_b32_e32 v155, 0xffff0000, v117
	v_pk_mul_f32 v[152:153], v[152:153], v[154:155]
	v_lshlrev_b32_e32 v154, 16, v125
	v_and_b32_e32 v155, 0xffff0000, v125
	v_lshlrev_b32_e32 v156, 16, v133
	v_and_b32_e32 v157, 0xffff0000, v133
	v_pk_mul_f32 v[154:155], v[154:155], v[156:157]
	v_pk_mul_f32 v[152:153], v[54:55], v[152:153]
	v_pk_fma_f32 v[152:153], v[70:71], v[150:151], v[152:153]
	v_pk_fma_f32 v[152:153], v[38:39], v[154:155], v[152:153]
	v_lshlrev_b32_e32 v156, 16, v85
	v_and_b32_e32 v157, 0xffff0000, v85
	v_pk_mul_f32 v[162:163], v[156:157], v[152:153]
	v_fmac_f32_e32 v158, v162, v162
	v_fmac_f32_e32 v158, v163, v163
	v_lshlrev_b32_e32 v150, 16, v94
	v_and_b32_e32 v151, 0xffff0000, v94
	v_lshlrev_b32_e32 v152, 16, v102
	v_and_b32_e32 v153, 0xffff0000, v102
	v_pk_mul_f32 v[150:151], v[150:151], v[152:153]
	v_lshlrev_b32_e32 v152, 16, v110
	v_and_b32_e32 v153, 0xffff0000, v110
	v_lshlrev_b32_e32 v154, 16, v118
	v_and_b32_e32 v155, 0xffff0000, v118
	v_pk_mul_f32 v[152:153], v[152:153], v[154:155]
	v_lshlrev_b32_e32 v154, 16, v126
	v_and_b32_e32 v155, 0xffff0000, v126
	v_lshlrev_b32_e32 v156, 16, v134
	v_and_b32_e32 v157, 0xffff0000, v134
	v_pk_mul_f32 v[154:155], v[154:155], v[156:157]
	v_pk_mul_f32 v[152:153], v[56:57], v[152:153]
	v_pk_fma_f32 v[152:153], v[72:73], v[150:151], v[152:153]
	v_pk_fma_f32 v[152:153], v[40:41], v[154:155], v[152:153]
	v_lshlrev_b32_e32 v156, 16, v86
	v_and_b32_e32 v157, 0xffff0000, v86
	v_pk_mul_f32 v[164:165], v[156:157], v[152:153]
	v_fmac_f32_e32 v158, v164, v164
	v_fmac_f32_e32 v158, v165, v165
	v_lshlrev_b32_e32 v150, 16, v95
	v_and_b32_e32 v151, 0xffff0000, v95
	v_lshlrev_b32_e32 v152, 16, v103
	v_and_b32_e32 v153, 0xffff0000, v103
	v_pk_mul_f32 v[150:151], v[150:151], v[152:153]
	v_lshlrev_b32_e32 v152, 16, v111
	v_and_b32_e32 v153, 0xffff0000, v111
	v_lshlrev_b32_e32 v154, 16, v119
	v_and_b32_e32 v155, 0xffff0000, v119
	v_pk_mul_f32 v[152:153], v[152:153], v[154:155]
	v_lshlrev_b32_e32 v154, 16, v127
	v_and_b32_e32 v155, 0xffff0000, v127
	v_lshlrev_b32_e32 v156, 16, v135
	v_and_b32_e32 v157, 0xffff0000, v135
	v_pk_mul_f32 v[154:155], v[154:155], v[156:157]
	v_pk_mul_f32 v[152:153], v[58:59], v[152:153]
	v_pk_fma_f32 v[152:153], v[74:75], v[150:151], v[152:153]
	v_pk_fma_f32 v[152:153], v[42:43], v[154:155], v[152:153]
	v_lshlrev_b32_e32 v156, 16, v87
	v_and_b32_e32 v157, 0xffff0000, v87
	v_pk_mul_f32 v[166:167], v[156:157], v[152:153]
	v_fmac_f32_e32 v158, v166, v166
	v_fmac_f32_e32 v158, v167, v167
	v_lshlrev_b32_e32 v150, 16, v96
	v_and_b32_e32 v151, 0xffff0000, v96
	v_lshlrev_b32_e32 v152, 16, v104
	v_and_b32_e32 v153, 0xffff0000, v104
; __device__ __forceinline__ void postproj_row(int R, int lane, const bf16* __restrict__ proj, const float* __restrict__ conv_w, const float* __restrict__ g_conv, ...
;     ...
;         const u32x2 w = *(const u32x2*)(pr + O_KV + lane * 4);
;         float f[4] = {__uint_as_float(w.x << 16), __uint_as_float(w.x & 0xffff0000u), __uint_as_float(w.y << 16), __uint_as_float(w.y & 0xffff0000u)};
;         const float ss = wave_sum(f[0] * f[0] + f[1] * f[1] + f[2] * f[2] + f[3] * f[3]);
;         const float rstd = rsqrtf(ss * (1.f / KVL) + EPS);
;         const f32x4 g = *(const f32x4*)(g_kv + lane * 4);
;         u32x2 o; o.x = pk2(f[0] * rstd * g.x, f[1] * rstd * g.y); o.y = pk2(f[2] * rstd * g.z, f[3] * rstd * g.w);
;         *(u32x2*)(kvn + (size_t)R * KVL + lane * 4) = o;
;     }
;     if (lane < 32) {
;         const float x1 = bf2f(pr[O_R + lane]), x2 = bf2f(pr[O_R + 32 + lane]);
;         const float cs = cosT[pos * 32 + lane], sn = sinT[pos * 32 + lane];
;         const bf16 o1 = f2bf(x1 * cs - x2 * sn), o2 = f2bf(x1 * sn + x2 * cs);
;         if (!meta) { bf16* d = kpe + (size_t)(b * LP + pos) * ROPE; d[lane] = o1; d[32 + lane] = o2; }
;         else { bf16* d0 = kpe + (size_t)(0 * LP + pos) * ROPE; bf16* d1 = kpe + (size_t)(1 * LP + pos) * ROPE; d0[lane] = o1; d0[32 + lane] = o2; d1[lane] = o1; d1[32 + lane] = o2; }
;     }
;     if (meta) return;
;     {
;         float f[8]; unpack8(*(const u32x4*)(pr + O_Q + lane * 8), f);
;         float ss = 0.f;
; #pragma unroll
;         for (int i = 0; i < 8; ++i) ss += f[i] * f[i];
;         const float rstd = rsqrtf(wave_sum(ss) * (1.f / QL) + EPS);
;         const f32x4 g0 = *(const f32x4*)(g_q + lane * 8), g1 = *(const f32x4*)(g_q + lane * 8 + 4);
;         u32x4 o; o.x = pk2(f[0] * rstd * g0.x, f[1] * rstd * g0.y); o.y = pk2(f[2] * rstd * g0.z, f[3] * rstd * g0.w);
;         o.z = pk2(f[4] * rstd * g1.x, f[5] * rstd * g1.y); o.w = pk2(f[6] * rstd * g1.z, f[7] * rstd * g1.w);
;         *(u32x4*)(qn + (size_t)R * QL + lane * 8) = o;
;     }
;     {
;         const int r1 = (t >= 1) ? R - 1 : M + 15, r2 = (t >= 2) ? R - 2 : (t == 1 ? M + 15 : M + 14);
;         const bf16* p1 = proj + (size_t)r1 * DINP; const bf16* p2 = proj + (size_t)r2 * DINP;
;         const int c0 = lane * 16;
;         float v[16]; float ss = 0.f;
; #pragma unroll
;         for (int hh = 0; hh < 2; ++hh) {
	v_pk_mul_f32 v[150:151], v[150:151], v[152:153]
	v_lshlrev_b32_e32 v152, 16, v112
	v_and_b32_e32 v153, 0xffff0000, v112
	v_lshlrev_b32_e32 v154, 16, v120
	v_and_b32_e32 v155, 0xffff0000, v120
	v_pk_mul_f32 v[152:153], v[152:153], v[154:155]
	v_lshlrev_b32_e32 v154, 16, v128
	v_and_b32_e32 v155, 0xffff0000, v128
	v_lshlrev_b32_e32 v156, 16, v136
	v_and_b32_e32 v157, 0xffff0000, v136
	v_pk_mul_f32 v[154:155], v[154:155], v[156:157]
	v_pk_mul_f32 v[152:153], v[60:61], v[152:153]
	v_pk_fma_f32 v[152:153], v[76:77], v[150:151], v[152:153]
	v_pk_fma_f32 v[152:153], v[44:45], v[154:155], v[152:153]
	v_lshlrev_b32_e32 v156, 16, v88
	v_and_b32_e32 v157, 0xffff0000, v88
	v_pk_mul_f32 v[168:169], v[156:157], v[152:153]
	v_fmac_f32_e32 v158, v168, v168
	v_fmac_f32_e32 v158, v169, v169
	v_lshlrev_b32_e32 v150, 16, v97
	v_and_b32_e32 v151, 0xffff0000, v97
	v_lshlrev_b32_e32 v152, 16, v105
	v_and_b32_e32 v153, 0xffff0000, v105
	v_pk_mul_f32 v[150:151], v[150:151], v[152:153]
	v_lshlrev_b32_e32 v152, 16, v113
	v_and_b32_e32 v153, 0xffff0000, v113
	v_lshlrev_b32_e32 v154, 16, v121
	v_and_b32_e32 v155, 0xffff0000, v121
	v_pk_mul_f32 v[152:153], v[152:153], v[154:155]
	v_lshlrev_b32_e32 v154, 16, v129
	v_and_b32_e32 v155, 0xffff0000, v129
	v_lshlrev_b32_e32 v156, 16, v137
	v_and_b32_e32 v157, 0xffff0000, v137
	v_pk_mul_f32 v[154:155], v[154:155], v[156:157]
	v_pk_mul_f32 v[152:153], v[62:63], v[152:153]
	v_pk_fma_f32 v[152:153], v[78:79], v[150:151], v[152:153]
	v_pk_fma_f32 v[152:153], v[46:47], v[154:155], v[152:153]
	v_lshlrev_b32_e32 v156, 16, v89
	v_and_b32_e32 v157, 0xffff0000, v89
	v_pk_mul_f32 v[170:171], v[156:157], v[152:153]
	v_fmac_f32_e32 v158, v170, v170
	v_fmac_f32_e32 v158, v171, v171
	v_lshlrev_b32_e32 v150, 16, v98
	v_and_b32_e32 v151, 0xffff0000, v98
	v_lshlrev_b32_e32 v152, 16, v106
	v_and_b32_e32 v153, 0xffff0000, v106
	v_pk_mul_f32 v[150:151], v[150:151], v[152:153]
	v_lshlrev_b32_e32 v152, 16, v114
	v_and_b32_e32 v153, 0xffff0000, v114
	v_lshlrev_b32_e32 v154, 16, v122
	v_and_b32_e32 v155, 0xffff0000, v122
	v_pk_mul_f32 v[152:153], v[152:153], v[154:155]
	v_lshlrev_b32_e32 v154, 16, v130
	v_and_b32_e32 v155, 0xffff0000, v130
	v_lshlrev_b32_e32 v156, 16, v138
	v_and_b32_e32 v157, 0xffff0000, v138
	v_pk_mul_f32 v[154:155], v[154:155], v[156:157]
	v_pk_mul_f32 v[152:153], v[64:65], v[152:153]
	v_pk_fma_f32 v[152:153], v[80:81], v[150:151], v[152:153]
	v_pk_fma_f32 v[152:153], v[48:49], v[154:155], v[152:153]
	v_lshlrev_b32_e32 v156, 16, v90
	v_and_b32_e32 v157, 0xffff0000, v90
	v_pk_mul_f32 v[172:173], v[156:157], v[152:153]
	v_fmac_f32_e32 v158, v172, v172
	v_fmac_f32_e32 v158, v173, v173
	v_lshlrev_b32_e32 v150, 16, v99
	v_and_b32_e32 v151, 0xffff0000, v99
	v_lshlrev_b32_e32 v152, 16, v107
	v_and_b32_e32 v153, 0xffff0000, v107
	v_pk_mul_f32 v[150:151], v[150:151], v[152:153]
	v_lshlrev_b32_e32 v152, 16, v115
	v_and_b32_e32 v153, 0xffff0000, v115
	v_lshlrev_b32_e32 v154, 16, v123
	v_and_b32_e32 v155, 0xffff0000, v123
	v_pk_mul_f32 v[152:153], v[152:153], v[154:155]
	v_lshlrev_b32_e32 v154, 16, v131
	v_and_b32_e32 v155, 0xffff0000, v131
	v_lshlrev_b32_e32 v156, 16, v139
	v_and_b32_e32 v157, 0xffff0000, v139
	v_pk_mul_f32 v[154:155], v[154:155], v[156:157]
	v_pk_mul_f32 v[152:153], v[66:67], v[152:153]
	v_pk_fma_f32 v[152:153], v[82:83], v[150:151], v[152:153]
	v_pk_fma_f32 v[152:153], v[50:51], v[154:155], v[152:153]
	v_lshlrev_b32_e32 v156, 16, v91
	v_and_b32_e32 v157, 0xffff0000, v91
	v_pk_mul_f32 v[174:175], v[156:157], v[152:153]
	v_fmac_f32_e32 v158, v174, v174
	v_fmac_f32_e32 v158, v175, v175
	v_readlane_b32 s43, v194, 63
	v_readlane_b32 s53, v195, 63
	s_nop 0
	v_add_f32_dpp v158, v158, v158 quad_perm:[1,0,3,2] row_mask:0xf bank_mask:0xf
	v_mov_b32_e32 v151, s43
	v_mov_b32_e32 v152, s53
	v_add_f32_dpp v158, v158, v158 quad_perm:[2,3,0,1] row_mask:0xf bank_mask:0xf
	v_fmamk_f32 v151, v151, 0x3b000000, v206
	v_fmamk_f32 v152, v152, 0x3b800000, v206
	v_fmamk_f32 v158, v158, 0x3c800000, v206
	v_rsq_f32_e32 v151, v151
	v_rsq_f32_e32 v152, v152
	v_rsq_f32_e32 v158, v158
	s_nop 0
	v_mov_b32_e32 v159, v158
	v_mul_f32_e32 v186, v151, v186
	v_mul_f32_e32 v187, v151, v187
	v_mul_f32_e32 v188, v151, v188
	v_mul_f32_e32 v189, v151, v189
	v_mul_f32_e32 v190, v151, v190
	v_mul_f32_e32 v191, v151, v191
	v_mul_f32_e32 v192, v151, v192
	v_mul_f32_e32 v193, v151, v193
	v_mul_f32_e32 v186, v12, v186
	v_mul_f32_e32 v187, v13, v187
	v_mul_f32_e32 v188, v14, v188
	v_mul_f32_e32 v189, v15, v189
	v_mul_f32_e32 v190, v16, v190
	v_mul_f32_e32 v191, v17, v191
	v_mul_f32_e32 v192, v18, v192
	v_mul_f32_e32 v193, v19, v193
	v_cvt_pk_bf16_f32 v200, v186, v187
	v_cvt_pk_bf16_f32 v201, v188, v189
	v_cvt_pk_bf16_f32 v202, v190, v191
	v_cvt_pk_bf16_f32 v203, v192, v193
	global_store_dwordx4 v3, v[200:203], s[24:25]
	v_mul_f32_e32 v196, v152, v196
	v_mul_f32_e32 v197, v152, v197
	v_mul_f32_e32 v198, v152, v198
	v_mul_f32_e32 v199, v152, v199
	v_mul_f32_e32 v196, v8, v196
	v_mul_f32_e32 v197, v9, v197
	v_mul_f32_e32 v198, v10, v198
	v_mul_f32_e32 v199, v11, v199
	v_cvt_pk_bf16_f32 v204, v196, v197
	v_cvt_pk_bf16_f32 v205, v198, v199
	global_store_dwordx2 v4, v[204:205], s[8:9]
	v_pk_mul_f32 v[160:161], v[160:161], v[158:159]
	v_pk_mul_f32 v[162:163], v[162:163], v[158:159]
	v_pk_mul_f32 v[164:165], v[164:165], v[158:159]
	v_pk_mul_f32 v[166:167], v[166:167], v[158:159]
	v_pk_mul_f32 v[168:169], v[168:169], v[158:159]
	v_pk_mul_f32 v[170:171], v[170:171], v[158:159]
	v_pk_mul_f32 v[172:173], v[172:173], v[158:159]
	v_pk_mul_f32 v[174:175], v[174:175], v[158:159]
	v_pk_mul_f32 v[160:161], v[160:161], v[20:21]
	v_pk_mul_f32 v[162:163], v[162:163], v[22:23]
	v_pk_mul_f32 v[164:165], v[164:165], v[24:25]
	v_pk_mul_f32 v[166:167], v[166:167], v[26:27]
	v_pk_mul_f32 v[168:169], v[168:169], v[28:29]
	v_pk_mul_f32 v[170:171], v[170:171], v[30:31]
	v_pk_mul_f32 v[172:173], v[172:173], v[32:33]
	v_pk_mul_f32 v[174:175], v[174:175], v[34:35]
	v_cvt_pk_bf16_f32 v178, v160, v161
	v_cvt_pk_bf16_f32 v179, v162, v163
	v_cvt_pk_bf16_f32 v180, v164, v165
	v_cvt_pk_bf16_f32 v181, v166, v167
	v_cvt_pk_bf16_f32 v182, v168, v169
	v_cvt_pk_bf16_f32 v183, v170, v171
	v_cvt_pk_bf16_f32 v184, v172, v173
	v_cvt_pk_bf16_f32 v185, v174, v175
	global_store_dwordx4 v2, v[178:181], s[6:7]
	global_store_dwordx4 v2, v[182:185], s[6:7] offset:16
	v_lshlrev_b32_e32 v146, 16, v146
	v_lshlrev_b32_e32 v147, 16, v147
	v_mul_f32_e32 v153, v149, v147
	v_mul_f32_e32 v154, v148, v147
	v_fma_f32 v153, v148, v146, -v153
	v_fmac_f32_e32 v154, v149, v146
	v_cvt_pk_bf16_f32 v155, v153, v154
	s_mov_b32 exec_hi, 0
	global_store_short v6, v155, s[10:11]
	global_store_short_d16_hi v6, v155, s[10:11] offset:64
	s_mov_b32 exec_hi, -1
	s_add_i32 s42, s42, s30
	s_cmpk_lt_i32 s42, 0x2000
	s_cbranch_scc1 .Lp2_loop
; __device__ __forceinline__ float bf2f(bf16 v) { return __uint_as_float((unsigned)v << 16); }
; __device__ __forceinline__ bf16 f2bf(float f) { unsigned u = __float_as_uint(f); return (bf16)((u + 0x7fffu + ((u >> 16) & 1u)) >> 16); }
; __device__ __forceinline__ unsigned pk2(float lo, float hi) { return (unsigned)f2bf(lo) | ((unsigned)f2bf(hi) << 16); }
; __device__ __forceinline__ void postproj_row(int R, int lane, const bf16* __restrict__ proj, const float* __restrict__ conv_w, const float* __restrict__ g_conv, ...
;     ...
;     const bool meta = R >= M; const int b = meta ? 0 : R / S, t = meta ? 0 : R % S, pos = meta ? R - M : t + NMETA;
;     {
;         const u32x2 w = *(const u32x2*)(pr + O_KV + lane * 4);
;         float f[4] = {__uint_as_float(w.x << 16), __uint_as_float(w.x & 0xffff0000u), __uint_as_float(w.y << 16), __uint_as_float(w.y & 0xffff0000u)};
;         const float ss = wave_sum(f[0] * f[0] + f[1] * f[1] + f[2] * f[2] + f[3] * f[3]);
;         const float rstd = rsqrtf(ss * (1.f / KVL) + EPS);
;         const f32x4 g = *(const f32x4*)(g_kv + lane * 4);
;         u32x2 o; o.x = pk2(f[0] * rstd * g.x, f[1] * rstd * g.y); o.y = pk2(f[2] * rstd * g.z, f[3] * rstd * g.w);
;         *(u32x2*)(kvn + (size_t)R * KVL + lane * 4) = o;
;     }
;     if (lane < 32) {
;         const float x1 = bf2f(pr[O_R + lane]), x2 = bf2f(pr[O_R + 32 + lane]);
;         const float cs = cosT[pos * 32 + lane], sn = sinT[pos * 32 + lane];
;         const bf16 o1 = f2bf(x1 * cs - x2 * sn), o2 = f2bf(x1 * sn + x2 * cs);
;         if (!meta) { bf16* d = kpe + (size_t)(b * LP + pos) * ROPE; d[lane] = o1; d[32 + lane] = o2; }
;         else { bf16* d0 = kpe + (size_t)(0 * LP + pos) * ROPE; bf16* d1 = kpe + (size_t)(1 * LP + pos) * ROPE; d0[lane] = o1; d0[32 + lane] = o2; d1[lane] = o1; d1[32 + lane] = o2; }
;     }
;     if (meta) return;
.Lp2_meta_chk:
	s_cmpk_lt_i32 s42, 0x2010
	s_cbranch_scc0 .LBB0_400
	s_lshl_b32 s43, s42, 13
	s_add_u32 s50, s44, s43
	s_addc_u32 s51, s45, 0
	s_add_u32 s50, s50, 0x1000
	s_addc_u32 s51, s51, 0
	s_sub_i32 s52, s42, 0x2000
	s_lshl_b32 s53, s52, 7
	s_add_u32 s58, s40, s53
	s_addc_u32 s59, s41, 0
	s_add_u32 s4, s58, 0x100000
	s_addc_u32 s5, s59, 0
	global_load_dwordx2 v[144:145], v4, s[50:51] offset:3072
	global_load_ushort v146, v6, s[50:51] offset:3584
	global_load_ushort v147, v6, s[50:51] offset:3648
	global_load_dword v148, v5, s[58:59]
	global_load_dword v149, v5, s[4:5]
	s_lshl_b32 s43, s42, 9
	s_add_u32 s8, s38, s43
	s_addc_u32 s9, s39, 0
	s_add_u32 s10, s26, s53
	s_addc_u32 s11, s27, 0
	s_add_u32 s6, s10, 0x84000
	s_addc_u32 s7, s11, 0
	v_mov_b32_e32 v206, 0x358637bd
	s_waitcnt vmcnt(0)
	v_lshlrev_b32_e32 v196, 16, v144
	v_and_b32_e32 v197, 0xffff0000, v144
	v_lshlrev_b32_e32 v198, 16, v145
	v_and_b32_e32 v199, 0xffff0000, v145
	v_mul_f32_e32 v195, v196, v196
	v_fmac_f32_e32 v195, v197, v197
	v_fmac_f32_e32 v195, v198, v198
	v_fmac_f32_e32 v195, v199, v199
	s_nop 1
	v_add_f32_dpp v195, v195, v195 quad_perm:[1,0,3,2] row_mask:0xf bank_mask:0xf
	s_nop 1
	v_add_f32_dpp v195, v195, v195 quad_perm:[2,3,0,1] row_mask:0xf bank_mask:0xf
	s_nop 1
	v_add_f32_dpp v195, v195, v195 row_half_mirror row_mask:0xf bank_mask:0xf
	s_nop 1
	v_add_f32_dpp v195, v195, v195 row_mirror row_mask:0xf bank_mask:0xf
	s_nop 1
	v_add_f32_dpp v195, v195, v195 row_bcast:15 row_mask:0xa bank_mask:0xf
	s_nop 1
	v_add_f32_dpp v195, v195, v195 row_bcast:31 row_mask:0xc bank_mask:0xf
	s_nop 1
	v_readlane_b32 s53, v195, 63
	s_nop 1
	v_mov_b32_e32 v152, s53
	v_fmamk_f32 v152, v152, 0x3b800000, v206
	v_rsq_f32_e32 v152, v152
	s_nop 0
	v_mul_f32_e32 v196, v152, v196
	v_mul_f32_e32 v197, v152, v197
	v_mul_f32_e32 v198, v152, v198
	v_mul_f32_e32 v199, v152, v199
	v_mul_f32_e32 v196, v8, v196
	v_mul_f32_e32 v197, v9, v197
	v_mul_f32_e32 v198, v10, v198
	v_mul_f32_e32 v199, v11, v199
	v_cvt_pk_bf16_f32 v204, v196, v197
	v_cvt_pk_bf16_f32 v205, v198, v199
	global_store_dwordx2 v4, v[204:205], s[8:9]
	v_lshlrev_b32_e32 v146, 16, v146
	v_lshlrev_b32_e32 v147, 16, v147
	v_mul_f32_e32 v153, v149, v147
	v_mul_f32_e32 v154, v148, v147
	v_fma_f32 v153, v148, v146, -v153
	v_fmac_f32_e32 v154, v149, v146
	v_cvt_pk_bf16_f32 v155, v153, v154
	s_mov_b32 exec_hi, 0
	global_store_short v6, v155, s[10:11]
	global_store_short_d16_hi v6, v155, s[10:11] offset:64
	global_store_short v6, v155, s[6:7]
	global_store_short_d16_hi v6, v155, s[6:7] offset:64
	s_mov_b32 exec_hi, -1
	s_add_i32 s42, s42, s30
	s_branch .Lp2_meta_chk
